# grid barrier: waiting workgroups poll the top generation word directly instead of the per-XCD word (one fewer memory hop per barrier)
# speedup vs baseline: 1.0027x; 1.0027x over previous
; __device__ __forceinline__ unsigned xb_ld(unsigned* p)              { return __hip_atomic_load(p, __ATOMIC_RELAXED, __HIP_MEMORY_SCOPE_AGENT); }
; __device__ __forceinline__ unsigned xb_add(unsigned* p, unsigned v) { return __hip_atomic_fetch_add(p, v, __ATOMIC_RELAXED, __HIP_MEMORY_SCOPE_AGENT); }
; #define XB_SPIN(cond, bar) do { unsigned _sp = 0; while (cond) { __builtin_amdgcn_s_sleep(1); \
;     if ((++_sp & 255u) == 0u) { if (xb_ld(&(bar)[XB_TMO])) break; if (_sp > XB_SPIN_CAP) { atomicAdd(&(bar)[XB_TMO], 1u); break; } } } } while (0)
; __device__ __forceinline__ void xcd_barrier(const XcdBarrier& b) {
;     ...
;         const unsigned old = xb_add(&bar[XB_XSUB(b.x)], 1u);
;         const unsigned gen = old / nloc;
;         if (old + 1u == (gen + 1u) * nloc) {
;             __builtin_amdgcn_fence(__ATOMIC_RELEASE, "agent");
;             asm volatile("s_waitcnt vmcnt(0)" ::: "memory");
;             const unsigned og = xb_add(&bar[XB_TOP], 1u);
;             const unsigned tg = og / nx;
;             if (og + 1u == (tg + 1u) * nx) xb_add(&bar[XB_TOPGEN], 1u);
;             else XB_SPIN(xb_ld(&bar[XB_TOPGEN]) == tg, bar);
;             __builtin_amdgcn_fence(__ATOMIC_ACQUIRE, "agent");
;             xb_add(&bar[XB_XGEN(b.x)], 1u);
;             asm volatile("s_waitcnt vmcnt(0)" ::: "memory");
;         } else {
;             XB_SPIN(xb_ld(&bar[XB_XGEN(b.x)]) == gen, bar);
.LBB0_348:
	v_readlane_b32 s8, v254, 8
	v_readlane_b32 s9, v254, 9
	v_cvt_f32_u32_e32 v1, v2
	v_sub_u32_e32 v4, 0, v2
	v_rcp_iflag_f32_e32 v1, v1
	s_nop 1
	global_atomic_add v3, v193, v226, s[8:9] sc0
	v_mul_f32_e32 v1, 0x4f7ffffe, v1
	v_cvt_u32_f32_e32 v1, v1
	v_mul_lo_u32 v4, v4, v1
	v_mul_hi_u32 v4, v1, v4
	v_add_u32_e32 v1, v1, v4
	s_waitcnt vmcnt(0)
	v_mul_hi_u32 v1, v3, v1
	v_mul_lo_u32 v4, v1, v2
	v_sub_u32_e32 v4, v3, v4
	v_add_u32_e32 v5, 1, v1
	v_cmp_ge_u32_e32 vcc, v4, v2
	v_add_u32_e32 v3, 1, v3
	s_nop 0
	v_cndmask_b32_e32 v1, v1, v5, vcc
	v_sub_u32_e32 v5, v4, v2
	v_cndmask_b32_e32 v4, v4, v5, vcc
	v_add_u32_e32 v5, 1, v1
	v_cmp_ge_u32_e32 vcc, v4, v2
	s_nop 1
	v_cndmask_b32_e32 v1, v1, v5, vcc
	v_mul_lo_u32 v4, v2, v1
	v_add_u32_e32 v2, v4, v2
	v_cmp_ne_u32_e32 vcc, v3, v2
	s_and_saveexec_b64 s[18:19], vcc
	s_xor_b64 s[36:37], exec, s[18:19]
	s_cbranch_execz .LBB0_362
	v_readlane_b32 s8, v254, 14
	v_readlane_b32 s9, v254, 15
	s_waitcnt lgkmcnt(0)
	s_nop 3
	global_load_dword v0, v193, s[8:9] sc1
	s_waitcnt vmcnt(0)
	v_cmp_eq_u32_e32 vcc, v0, v1
	s_and_saveexec_b64 s[38:39], vcc
	s_cbranch_execz .LBB0_361
	s_mov_b32 s5, 1
	s_mov_b64 s[40:41], 0
	s_branch .LBB0_352

; __device__ __forceinline__ unsigned xb_ld(unsigned* p)              { return __hip_atomic_load(p, __ATOMIC_RELAXED, __HIP_MEMORY_SCOPE_AGENT); }
; #define XB_SPIN(cond, bar) do { unsigned _sp = 0; while (cond) { __builtin_amdgcn_s_sleep(1); \
;     if ((++_sp & 255u) == 0u) { if (xb_ld(&(bar)[XB_TMO])) break; if (_sp > XB_SPIN_CAP) { atomicAdd(&(bar)[XB_TMO], 1u); break; } } } } while (0)
; __device__ __forceinline__ void xcd_barrier(const XcdBarrier& b) {
;     ...
;             XB_SPIN(xb_ld(&bar[XB_XGEN(b.x)]) == gen, bar);
.LBB0_356:
	v_readlane_b32 s8, v254, 14
	v_readlane_b32 s9, v254, 15
	s_add_i32 s5, s5, 1
	s_mov_b64 s[46:47], -1
	s_nop 2
	global_load_dword v0, v193, s[8:9] sc1
	s_waitcnt vmcnt(0)
	v_cmp_ne_u32_e32 vcc, v0, v1
	s_orn2_b64 s[44:45], vcc, exec
	s_branch .LBB0_351

; __device__ __forceinline__ unsigned xb_ld(unsigned* p)              { return __hip_atomic_load(p, __ATOMIC_RELAXED, __HIP_MEMORY_SCOPE_AGENT); }
; __device__ __forceinline__ unsigned xb_add(unsigned* p, unsigned v) { return __hip_atomic_fetch_add(p, v, __ATOMIC_RELAXED, __HIP_MEMORY_SCOPE_AGENT); }
; #define XB_SPIN(cond, bar) do { unsigned _sp = 0; while (cond) { __builtin_amdgcn_s_sleep(1); \
;     if ((++_sp & 255u) == 0u) { if (xb_ld(&(bar)[XB_TMO])) break; if (_sp > XB_SPIN_CAP) { atomicAdd(&(bar)[XB_TMO], 1u); break; } } } } while (0)
; __device__ __forceinline__ void xcd_barrier(const XcdBarrier& b) {
;     ...
;         const unsigned old = xb_add(&bar[XB_XSUB(b.x)], 1u);
;         const unsigned gen = old / nloc;
;         if (old + 1u == (gen + 1u) * nloc) {
;             __builtin_amdgcn_fence(__ATOMIC_RELEASE, "agent");
;             asm volatile("s_waitcnt vmcnt(0)" ::: "memory");
;             const unsigned og = xb_add(&bar[XB_TOP], 1u);
;             const unsigned tg = og / nx;
;             if (og + 1u == (tg + 1u) * nx) xb_add(&bar[XB_TOPGEN], 1u);
;             else XB_SPIN(xb_ld(&bar[XB_TOPGEN]) == tg, bar);
;             __builtin_amdgcn_fence(__ATOMIC_ACQUIRE, "agent");
;             xb_add(&bar[XB_XGEN(b.x)], 1u);
;             asm volatile("s_waitcnt vmcnt(0)" ::: "memory");
;         } else {
;             XB_SPIN(xb_ld(&bar[XB_XGEN(b.x)]) == gen, bar);
.LBB0_878:
	v_readlane_b32 s8, v254, 8
	v_readlane_b32 s9, v254, 9
	v_cvt_f32_u32_e32 v1, v2
	v_sub_u32_e32 v4, 0, v2
	v_rcp_iflag_f32_e32 v1, v1
	s_nop 1
	global_atomic_add v3, v193, v226, s[8:9] sc0
	v_mul_f32_e32 v1, 0x4f7ffffe, v1
	v_cvt_u32_f32_e32 v1, v1
	v_mul_lo_u32 v4, v4, v1
	v_mul_hi_u32 v4, v1, v4
	v_add_u32_e32 v1, v1, v4
	s_waitcnt vmcnt(0)
	v_mul_hi_u32 v1, v3, v1
	v_mul_lo_u32 v4, v1, v2
	v_sub_u32_e32 v4, v3, v4
	v_add_u32_e32 v5, 1, v1
	v_cmp_ge_u32_e32 vcc, v4, v2
	v_add_u32_e32 v3, 1, v3
	s_nop 0
	v_cndmask_b32_e32 v1, v1, v5, vcc
	v_sub_u32_e32 v5, v4, v2
	v_cndmask_b32_e32 v4, v4, v5, vcc
	v_add_u32_e32 v5, 1, v1
	v_cmp_ge_u32_e32 vcc, v4, v2
	s_nop 1
	v_cndmask_b32_e32 v1, v1, v5, vcc
	v_mul_lo_u32 v4, v2, v1
	v_add_u32_e32 v2, v4, v2
	v_cmp_ne_u32_e32 vcc, v3, v2
	s_and_saveexec_b64 s[18:19], vcc
	s_xor_b64 s[20:21], exec, s[18:19]
	s_cbranch_execz .LBB0_892
	v_readlane_b32 s8, v254, 14
	v_readlane_b32 s9, v254, 15
	s_waitcnt lgkmcnt(0)
	s_nop 3
	global_load_dword v0, v193, s[8:9] sc1
	s_waitcnt vmcnt(0)
	v_cmp_eq_u32_e32 vcc, v0, v1
	s_and_saveexec_b64 s[36:37], vcc
	s_cbranch_execz .LBB0_891
	s_mov_b32 s5, 1
	s_mov_b64 s[38:39], 0
	s_branch .LBB0_882

; __device__ __forceinline__ unsigned xb_ld(unsigned* p)              { return __hip_atomic_load(p, __ATOMIC_RELAXED, __HIP_MEMORY_SCOPE_AGENT); }
; #define XB_SPIN(cond, bar) do { unsigned _sp = 0; while (cond) { __builtin_amdgcn_s_sleep(1); \
;     if ((++_sp & 255u) == 0u) { if (xb_ld(&(bar)[XB_TMO])) break; if (_sp > XB_SPIN_CAP) { atomicAdd(&(bar)[XB_TMO], 1u); break; } } } } while (0)
; __device__ __forceinline__ void xcd_barrier(const XcdBarrier& b) {
;     ...
;             XB_SPIN(xb_ld(&bar[XB_XGEN(b.x)]) == gen, bar);
.LBB0_886:
	v_readlane_b32 s8, v254, 14
	v_readlane_b32 s9, v254, 15
	s_add_i32 s5, s5, 1
	s_mov_b64 s[44:45], -1
	s_nop 2
	global_load_dword v0, v193, s[8:9] sc1
	s_waitcnt vmcnt(0)
	v_cmp_ne_u32_e32 vcc, v0, v1
	s_orn2_b64 s[42:43], vcc, exec
	s_branch .LBB0_881

; __device__ __forceinline__ unsigned xb_ld(unsigned* p)              { return __hip_atomic_load(p, __ATOMIC_RELAXED, __HIP_MEMORY_SCOPE_AGENT); }
; __device__ __forceinline__ unsigned xb_add(unsigned* p, unsigned v) { return __hip_atomic_fetch_add(p, v, __ATOMIC_RELAXED, __HIP_MEMORY_SCOPE_AGENT); }
; #define XB_SPIN(cond, bar) do { unsigned _sp = 0; while (cond) { __builtin_amdgcn_s_sleep(1); \
;     if ((++_sp & 255u) == 0u) { if (xb_ld(&(bar)[XB_TMO])) break; if (_sp > XB_SPIN_CAP) { atomicAdd(&(bar)[XB_TMO], 1u); break; } } } } while (0)
; __device__ __forceinline__ void xcd_barrier(const XcdBarrier& b) {
;     ...
;         const unsigned old = xb_add(&bar[XB_XSUB(b.x)], 1u);
;         const unsigned gen = old / nloc;
;         if (old + 1u == (gen + 1u) * nloc) {
;             __builtin_amdgcn_fence(__ATOMIC_RELEASE, "agent");
;             asm volatile("s_waitcnt vmcnt(0)" ::: "memory");
;             const unsigned og = xb_add(&bar[XB_TOP], 1u);
;             const unsigned tg = og / nx;
;             if (og + 1u == (tg + 1u) * nx) xb_add(&bar[XB_TOPGEN], 1u);
;             else XB_SPIN(xb_ld(&bar[XB_TOPGEN]) == tg, bar);
;             __builtin_amdgcn_fence(__ATOMIC_ACQUIRE, "agent");
;             xb_add(&bar[XB_XGEN(b.x)], 1u);
;             asm volatile("s_waitcnt vmcnt(0)" ::: "memory");
;         } else {
;             XB_SPIN(xb_ld(&bar[XB_XGEN(b.x)]) == gen, bar);
.LBB0_1489:
	v_readlane_b32 s8, v254, 8
	v_readlane_b32 s9, v254, 9
	v_cvt_f32_u32_e32 v1, v2
	v_sub_u32_e32 v4, 0, v2
	v_rcp_iflag_f32_e32 v1, v1
	s_nop 1
	global_atomic_add v3, v193, v226, s[8:9] sc0
	v_mul_f32_e32 v1, 0x4f7ffffe, v1
	v_cvt_u32_f32_e32 v1, v1
	v_mul_lo_u32 v4, v4, v1
	v_mul_hi_u32 v4, v1, v4
	v_add_u32_e32 v1, v1, v4
	s_waitcnt vmcnt(0)
	v_mul_hi_u32 v1, v3, v1
	v_mul_lo_u32 v4, v1, v2
	v_sub_u32_e32 v4, v3, v4
	v_add_u32_e32 v5, 1, v1
	v_cmp_ge_u32_e32 vcc, v4, v2
	v_add_u32_e32 v3, 1, v3
	s_nop 0
	v_cndmask_b32_e32 v1, v1, v5, vcc
	v_sub_u32_e32 v5, v4, v2
	v_cndmask_b32_e32 v4, v4, v5, vcc
	v_add_u32_e32 v5, 1, v1
	v_cmp_ge_u32_e32 vcc, v4, v2
	s_nop 1
	v_cndmask_b32_e32 v1, v1, v5, vcc
	v_mul_lo_u32 v4, v2, v1
	v_add_u32_e32 v2, v4, v2
	v_cmp_ne_u32_e32 vcc, v3, v2
	s_and_saveexec_b64 s[18:19], vcc
	s_xor_b64 s[20:21], exec, s[18:19]
	s_cbranch_execz .LBB0_1503
	v_readlane_b32 s8, v254, 14
	v_readlane_b32 s9, v254, 15
	s_waitcnt lgkmcnt(0)
	s_nop 3
	global_load_dword v0, v193, s[8:9] sc1
	s_waitcnt vmcnt(0)
	v_cmp_eq_u32_e32 vcc, v0, v1
	s_and_saveexec_b64 s[38:39], vcc
	s_cbranch_execz .LBB0_1502
	s_mov_b32 s5, 1
	s_mov_b64 s[40:41], 0
	s_branch .LBB0_1493

; __device__ __forceinline__ unsigned xb_ld(unsigned* p)              { return __hip_atomic_load(p, __ATOMIC_RELAXED, __HIP_MEMORY_SCOPE_AGENT); }
; __device__ __forceinline__ unsigned xb_add(unsigned* p, unsigned v) { return __hip_atomic_fetch_add(p, v, __ATOMIC_RELAXED, __HIP_MEMORY_SCOPE_AGENT); }
; #define XB_SPIN(cond, bar) do { unsigned _sp = 0; while (cond) { __builtin_amdgcn_s_sleep(1); \
;     if ((++_sp & 255u) == 0u) { if (xb_ld(&(bar)[XB_TMO])) break; if (_sp > XB_SPIN_CAP) { atomicAdd(&(bar)[XB_TMO], 1u); break; } } } } while (0)
; __device__ __forceinline__ void xcd_barrier(const XcdBarrier& b) {
;     ...
;         const unsigned old = xb_add(&bar[XB_XSUB(b.x)], 1u);
;         const unsigned gen = old / nloc;
;         if (old + 1u == (gen + 1u) * nloc) {
;             __builtin_amdgcn_fence(__ATOMIC_RELEASE, "agent");
;             asm volatile("s_waitcnt vmcnt(0)" ::: "memory");
;             const unsigned og = xb_add(&bar[XB_TOP], 1u);
;             const unsigned tg = og / nx;
;             if (og + 1u == (tg + 1u) * nx) xb_add(&bar[XB_TOPGEN], 1u);
;             else XB_SPIN(xb_ld(&bar[XB_TOPGEN]) == tg, bar);
;             __builtin_amdgcn_fence(__ATOMIC_ACQUIRE, "agent");
;             xb_add(&bar[XB_XGEN(b.x)], 1u);
;             asm volatile("s_waitcnt vmcnt(0)" ::: "memory");
;         } else {
;             XB_SPIN(xb_ld(&bar[XB_XGEN(b.x)]) == gen, bar);
.LBB0_1713:
	v_readlane_b32 s4, v254, 8
	v_readlane_b32 s5, v254, 9
	v_cvt_f32_u32_e32 v1, v2
	v_sub_u32_e32 v4, 0, v2
	v_rcp_iflag_f32_e32 v1, v1
	s_nop 1
	global_atomic_add v3, v193, v226, s[4:5] sc0
	v_mul_f32_e32 v1, 0x4f7ffffe, v1
	v_cvt_u32_f32_e32 v1, v1
	v_mul_lo_u32 v4, v4, v1
	v_mul_hi_u32 v4, v1, v4
	v_add_u32_e32 v1, v1, v4
	s_waitcnt vmcnt(0)
	v_mul_hi_u32 v1, v3, v1
	v_mul_lo_u32 v4, v1, v2
	v_sub_u32_e32 v4, v3, v4
	v_add_u32_e32 v5, 1, v1
	v_cmp_ge_u32_e32 vcc, v4, v2
	v_add_u32_e32 v3, 1, v3
	s_nop 0
	v_cndmask_b32_e32 v1, v1, v5, vcc
	v_sub_u32_e32 v5, v4, v2
	v_cndmask_b32_e32 v4, v4, v5, vcc
	v_add_u32_e32 v5, 1, v1
	v_cmp_ge_u32_e32 vcc, v4, v2
	s_nop 1
	v_cndmask_b32_e32 v1, v1, v5, vcc
	v_mul_lo_u32 v4, v2, v1
	v_add_u32_e32 v2, v4, v2
	v_cmp_ne_u32_e32 vcc, v3, v2
	s_and_saveexec_b64 s[4:5], vcc
	s_xor_b64 s[18:19], exec, s[4:5]
	s_cbranch_execz .LBB0_1727
	v_readlane_b32 s4, v254, 14
	v_readlane_b32 s5, v254, 15
	s_waitcnt lgkmcnt(0)
	s_nop 3
	global_load_dword v0, v193, s[4:5] sc1
	s_waitcnt vmcnt(0)
	v_cmp_eq_u32_e32 vcc, v0, v1
	s_and_saveexec_b64 s[20:21], vcc
	s_cbranch_execz .LBB0_1726
	s_mov_b32 s4, 1
	s_mov_b64 s[36:37], 0
	s_branch .LBB0_1717

; __device__ __forceinline__ unsigned xb_ld(unsigned* p)              { return __hip_atomic_load(p, __ATOMIC_RELAXED, __HIP_MEMORY_SCOPE_AGENT); }
; #define XB_SPIN(cond, bar) do { unsigned _sp = 0; while (cond) { __builtin_amdgcn_s_sleep(1); \
;     if ((++_sp & 255u) == 0u) { if (xb_ld(&(bar)[XB_TMO])) break; if (_sp > XB_SPIN_CAP) { atomicAdd(&(bar)[XB_TMO], 1u); break; } } } } while (0)
; __device__ __forceinline__ void xcd_barrier(const XcdBarrier& b) {
;     ...
;             XB_SPIN(xb_ld(&bar[XB_XGEN(b.x)]) == gen, bar);
.LBB0_1721:
	v_readlane_b32 s8, v254, 14
	v_readlane_b32 s9, v254, 15
	s_add_i32 s4, s4, 1
	s_mov_b64 s[42:43], -1
	s_nop 2
	global_load_dword v0, v193, s[8:9] sc1
	s_waitcnt vmcnt(0)
	v_cmp_ne_u32_e32 vcc, v0, v1
	s_orn2_b64 s[40:41], vcc, exec
	s_branch .LBB0_1716
